# baseline (speedup 1.0000x reference)
_ZN12_GLOBAL__N_113search_kernelEPKfS1_PhPf:
	s_load_dwordx2 s[8:9], s[0:1], 0x0
	s_load_dwordx2 s[4:5], s[0:1], 0x10
	s_movk_i32 s3, 0x90
	v_readfirstlane_b32 s10, v0
	v_cmp_gt_u32_e32 vcc, s3, v0
	s_and_saveexec_b64 s[6:7], vcc
	v_mov_b32_e32 v2, -1
	v_lshlrev_b32_e32 v1, 3, v0
	v_mov_b32_e32 v3, v2
	ds_write_b64 v1, v[2:3] offset:16384
	s_or_b64 exec, exec, s[6:7]
	s_waitcnt lgkmcnt(0)
	s_add_u32 s6, s4, 0x240000
	s_addc_u32 s7, s5, 0
	s_lshl_b32 s11, s2, 1
	s_and_b32 s14, s11, 14
	s_ashr_i32 s11, s2, 7
	s_lshr_b32 s15, s10, 6
	s_add_i32 s14, s14, s11
	s_bfe_u32 s2, s2, 0x40003
	s_mul_i32 s11, s15, 24
	v_mul_u32_u24_e32 v2, 0x71d, v0
	v_mul_u32_u24_e32 v4, 0x195, v0
	s_min_u32 s18, s11, 0xa5
	s_mul_i32 s11, s14, 3
	s_mul_i32 s12, s2, 9
	s_mov_b32 s13, 0
	v_lshrrev_b32_e32 v3, 16, v2
	s_movk_i32 s19, 0xffdc
	v_lshrrev_b32_e32 v5, 17, v4
	v_mad_i32_i24 v2, v3, s19, v0
	v_mad_i32_i24 v4, v5, -9, v3
	v_add_u32_e32 v3, s11, v5
	v_mov_b64_e32 v[6:7], s[12:13]
	v_mad_i64_i32 v[8:9], s[16:17], v3, s3, v[6:7]
	v_ashrrev_i32_e32 v5, 31, v4
	v_lshl_add_u64 v[4:5], v[8:9], 0, v[4:5]
	s_movk_i32 s13, 0x240
	v_mov_b64_e32 v[8:9], s[8:9]
	v_mad_u64_u32 v[10:11], s[8:9], v4, s13, v[8:9]
	v_min_u32_e32 v4, 0x1cb, v0
	v_or_b32_e32 v4, 0x200, v4
	v_mad_i32_i24 v11, v5, s13, v11
	v_mul_u32_u24_e32 v5, 0x71d, v4
	v_ashrrev_i32_e32 v3, 31, v2
	v_lshrrev_b32_e32 v5, 16, v5
	v_lshl_add_u64 v[2:3], v[2:3], 4, v[10:11]
	v_mad_i32_i24 v10, v5, s19, v4
	v_mul_u32_u24_e32 v4, 0x653, v4
	v_lshrrev_b32_e32 v11, 19, v4
	v_mad_i32_i24 v4, v11, -9, v5
	v_add_u32_e32 v5, s11, v11
	v_mad_i64_i32 v[6:7], s[8:9], v5, s3, v[6:7]
	v_ashrrev_i32_e32 v5, 31, v4
	v_lshl_add_u64 v[4:5], v[6:7], 0, v[4:5]
	v_mad_u64_u32 v[12:13], s[8:9], v4, s13, v[8:9]
	s_mul_i32 s8, s14, 0x90
	s_barrier
	s_load_dwordx2 s[42:43], s[0:1], 0x8
	s_load_dwordx2 s[62:63], s[0:1], 0x0
	v_mov_b32_e32 v244, v2
	v_mov_b32_e32 v245, v3
	global_load_dwordx4 v[6:9], v[2:3], off
	v_mad_i32_i24 v13, v5, s13, v13
	v_ashrrev_i32_e32 v11, 31, v10
	v_lshl_add_u64 v[10:11], v[10:11], 4, v[12:13]
	v_mov_b32_e32 v246, v10
	v_mov_b32_e32 v247, v11
	global_load_dwordx4 v[10:13], v[10:11], off
	v_and_b32_e32 v1, 63, v0
	s_add_i32 s20, s8, s12
	s_lshl_b32 s20, s20, 10
	v_lshl_add_u32 v164, v1, 4, s20
	s_mul_i32 s9, s14, 0xbd
	s_add_i32 s21, s9, s18
	s_lshl_b32 s21, s21, 10
	v_lshl_add_u32 v165, v1, 4, s21
	s_add_u32 s22, s4, 0x1000
	s_addc_u32 s23, s5, 0
	s_add_u32 s24, s4, 0x2000
	s_addc_u32 s25, s5, 0
	s_mov_b32 s26, s6
	s_mov_b32 s27, s7
	s_add_u32 s28, s6, 0x1000
	s_addc_u32 s29, s7, 0
	s_add_u32 s30, s6, 0x2000
	s_addc_u32 s31, s7, 0
	s_add_u32 s32, s6, 0x3000
	s_addc_u32 s33, s7, 0
	s_add_u32 s34, s6, 0x4000
	s_addc_u32 s35, s7, 0
	s_add_u32 s36, s6, 0x5000
	s_addc_u32 s37, s7, 0
	v_bfe_u32 v166, v0, 4, 2
	v_and_b32_e32 v167, 15, v0
	v_lshlrev_b32_e32 v167, 3, v167
	s_mul_i32 s40, s15, 6
	s_mov_b32 s41, 0x7f000000
	global_load_dwordx4 v[112:115], v164, s[4:5]
	global_load_dwordx4 v[16:19], v165, s[26:27] nt
	global_load_dwordx4 v[20:23], v165, s[26:27] offset:1024 nt
	global_load_dwordx4 v[24:27], v165, s[26:27] offset:2048 nt
	global_load_dwordx4 v[28:31], v165, s[26:27] offset:3072 nt
	global_load_dwordx4 v[32:35], v165, s[28:29] nt
	global_load_dwordx4 v[36:39], v165, s[28:29] offset:1024 nt
	global_load_dwordx4 v[40:43], v165, s[28:29] offset:2048 nt
	global_load_dwordx4 v[44:47], v165, s[28:29] offset:3072 nt
	global_load_dwordx4 v[48:51], v165, s[30:31] nt
	global_load_dwordx4 v[52:55], v165, s[30:31] offset:1024 nt
	global_load_dwordx4 v[56:59], v165, s[30:31] offset:2048 nt
	global_load_dwordx4 v[60:63], v165, s[30:31] offset:3072 nt
	global_load_dwordx4 v[64:67], v165, s[32:33] nt
	global_load_dwordx4 v[68:71], v165, s[32:33] offset:1024 nt
	global_load_dwordx4 v[72:75], v165, s[32:33] offset:2048 nt
	global_load_dwordx4 v[76:79], v165, s[32:33] offset:3072 nt
	global_load_dwordx4 v[80:83], v165, s[34:35] nt
	global_load_dwordx4 v[84:87], v165, s[34:35] offset:1024 nt
	global_load_dwordx4 v[88:91], v165, s[34:35] offset:2048 nt
	global_load_dwordx4 v[92:95], v165, s[34:35] offset:3072 nt
	global_load_dwordx4 v[96:99], v165, s[36:37] nt
	global_load_dwordx4 v[100:103], v165, s[36:37] offset:1024 nt
	global_load_dwordx4 v[104:107], v165, s[36:37] offset:2048 nt
	global_load_dwordx4 v[108:111], v165, s[36:37] offset:3072 nt
	global_load_dwordx4 v[116:119], v164, s[4:5] offset:1024
	v_lshlrev_b32_e32 v14, 4, v0
	s_lshr_b32 s50, s15, 1
	s_and_b32 s51, s15, 1
	s_lshl_b32 s51, s51, 3
	s_mov_b32 s48, 0x1010101
	s_mov_b32 s49, 0x1010101
	s_movk_i32 s58, 0x900
	s_movk_i32 s59, 0xb40
	v_and_b32_e32 v168, 7, v0
	v_lshrrev_b32_e32 v177, 3, v1
	v_or_b32_e32 v177, s51, v177
	v_lshlrev_b32_e32 v169, 3, v177
	v_and_b32_e32 v179, 3, v0
	v_lshlrev_b32_e32 v179, 8, v179
	v_lshl_add_u32 v170, v177, 4, v179
	v_add_u32_e32 v170, s20, v170
	v_lshrrev_b32_e32 v179, 2, v168
	v_and_b32_e32 v180, 3, v0
	v_lshl_or_b32 v171, v179, 4, v180
	v_mul_u32_u24_e32 v179, 11, v168
	v_lshrrev_b32_e32 v179, 5, v179
	v_mul_u32_u24_e32 v180, 3, v179
	v_sub_u32_e32 v180, v168, v180
	v_mul_u32_u24_e32 v181, 0x90, v179
	v_add_u32_e32 v181, v181, v180
	v_mul_u32_u24_e32 v172, 0x240, v181
	v_mul_u32_u24_e32 v181, 0x48, v179
	v_add_u32_e32 v181, v181, v180
	v_mul_u32_u24_e32 v173, 0x120, v181
	v_mul_u32_u24_e32 v181, 0x24, v179
	v_add_u32_e32 v181, v181, v180
	v_mul_u32_u24_e32 v174, 0x90, v181
	v_mul_u32_u24_e32 v181, 9, v179
	v_add_u32_e32 v181, v181, v180
	v_mul_u32_u24_e32 v175, 0x240, v181
	v_add_u32_e32 v176, 8, v168
	s_waitcnt lgkmcnt(0)
	s_mul_i32 s60, s14, 0x3cc00
	s_add_u32 s42, s42, s60
	s_addc_u32 s43, s43, 0
	s_mul_i32 s60, s14, 0xf300
	s_add_u32 s44, s4, s60
	s_addc_u32 s45, s5, 0
	s_add_u32 s44, s44, 0x534000
	s_addc_u32 s45, s45, 0
	s_mul_i32 s60, s14, 0x3cc0
	s_add_u32 s46, s4, s60
	s_addc_u32 s47, s5, 0
	s_add_u32 s46, s46, 0x627000
	s_addc_u32 s47, s47, 0
	v_mov_b32_e32 v152, s42
	v_mov_b32_e32 v153, s43
	v_mov_b32_e32 v154, s44
	v_mov_b32_e32 v155, s45
	v_mov_b32_e32 v159, s46
	v_mov_b32_e32 v161, s47
	s_sub_u32 s60, s42, s62
	s_subb_u32 s61, s43, s63
	s_mul_i32 s62, s14, 0x3cc00
	s_sub_u32 s60, s60, s62
	s_subb_u32 s61, s61, 0
	v_lshl_add_u64 v[244:245], v[244:245], 0, s[60:61]
	v_lshl_add_u64 v[246:247], v[246:247], 0, s[60:61]
	s_lshl_b32 s62, s15, 10
	s_add_i32 s62, s62, 0x46e0
	s_mov_b32 m0, s62
	s_mul_i32 s62, s2, 0xf30
	s_add_u32 s60, s44, s62
	s_addc_u32 s61, s45, 0
	v_lshlrev_b32_e32 v240, 4, v0
	v_mov_b32_e32 v241, 0
	v_lshl_add_u64 v[240:241], v[240:241], 0, s[60:61]
	s_mul_i32 s62, s2, 0x3cc
	s_add_u32 s60, s46, s62
	s_addc_u32 s61, s47, 0
	v_lshlrev_b32_e32 v242, 2, v0
	v_mov_b32_e32 v243, 0
	v_lshl_add_u64 v[242:243], v[242:243], 0, s[60:61]
	global_load_lds_dwordx4 v[244:245], off
	global_load_lds_dwordx4 v[246:247], off
	global_load_lds_dwordx4 v[240:241], off
	global_load_lds_dword v[242:243], off
	s_waitcnt vmcnt(25)
	ds_write_b128 v14, v[6:9]
	ds_write_b128 v14, v[10:13] offset:8192
	v_mfma_f32_16x16x32_f16 v[120:123], v[16:19], v[112:115], 0
	v_mfma_f32_16x16x32_f16 v[124:127], v[20:23], v[112:115], 0
	v_mfma_f32_16x16x32_f16 v[128:131], v[24:27], v[112:115], 0
	v_mfma_f32_16x16x32_f16 v[132:135], v[28:31], v[112:115], 0
	s_waitcnt vmcnt(21)
	v_mfma_f32_16x16x32_f16 v[136:139], v[32:35], v[112:115], 0
	v_mfma_f32_16x16x32_f16 v[140:143], v[36:39], v[112:115], 0
	v_mfma_f32_16x16x32_f16 v[144:147], v[40:43], v[112:115], 0
	v_mfma_f32_16x16x32_f16 v[148:151], v[44:47], v[112:115], 0
	v_min3_i32 v160, v120, v121, s41
	v_min3_i32 v160, v122, v123, v160
	v_min3_i32 v160, v124, v125, v160
	v_min3_i32 v160, v126, v127, v160
	v_min3_i32 v160, v128, v129, v160
	v_min3_i32 v160, v130, v131, v160
	v_min3_i32 v160, v132, v133, v160
	v_min3_i32 v157, v134, v135, v160
	v_mov_b32_e32 v6, 0
	v_mov_b32_e32 v7, 0x900
	v_mov_b32_e32 v8, 0x240
	s_waitcnt vmcnt(17)
	v_mfma_f32_16x16x32_f16 v[120:123], v[48:51], v[112:115], 0
	v_mfma_f32_16x16x32_f16 v[124:127], v[52:55], v[112:115], 0
	v_mov_b32_e32 v158, 0
	v_mfma_f32_16x16x32_f16 v[128:131], v[56:59], v[112:115], 0
	v_mfma_f32_16x16x32_f16 v[132:135], v[60:63], v[112:115], 0
	v_min3_i32 v160, v136, v137, v157
	v_min3_i32 v160, v138, v139, v160
	v_min3_i32 v160, v140, v141, v160
	v_min3_i32 v160, v142, v143, v160
	v_min3_i32 v160, v144, v145, v160
	v_min3_i32 v160, v146, v147, v160
	v_min3_i32 v160, v148, v149, v160
	v_min3_i32 v156, v150, v151, v160
	v_cmp_ge_i32_e32 vcc, v156, v157
	s_waitcnt vmcnt(13)
	v_mfma_f32_16x16x32_f16 v[136:139], v[64:67], v[112:115], 0
	v_mfma_f32_16x16x32_f16 v[140:143], v[68:71], v[112:115], 0
	v_cndmask_b32_e32 v158, 1, v158, vcc
	v_mfma_f32_16x16x32_f16 v[144:147], v[72:75], v[112:115], 0
	v_mfma_f32_16x16x32_f16 v[148:151], v[76:79], v[112:115], 0
	v_min3_i32 v160, v120, v121, v156
	v_min3_i32 v160, v122, v123, v160
	v_min3_i32 v160, v124, v125, v160
	v_min3_i32 v160, v126, v127, v160
	v_min3_i32 v160, v128, v129, v160
	v_min3_i32 v160, v130, v131, v160
	v_min3_i32 v160, v132, v133, v160
	v_min3_i32 v157, v134, v135, v160
	v_cmp_ge_i32_e32 vcc, v157, v156
	s_waitcnt vmcnt(9)
	v_mfma_f32_16x16x32_f16 v[120:123], v[80:83], v[112:115], 0
	v_mfma_f32_16x16x32_f16 v[124:127], v[84:87], v[112:115], 0
	v_cndmask_b32_e32 v158, 2, v158, vcc
	v_mfma_f32_16x16x32_f16 v[128:131], v[88:91], v[112:115], 0
	v_mfma_f32_16x16x32_f16 v[132:135], v[92:95], v[112:115], 0
	v_min3_i32 v160, v136, v137, v157
	v_min3_i32 v160, v138, v139, v160
	v_min3_i32 v160, v140, v141, v160
	v_min3_i32 v160, v142, v143, v160
	v_min3_i32 v160, v144, v145, v160
	v_min3_i32 v160, v146, v147, v160
	v_min3_i32 v160, v148, v149, v160
	v_min3_i32 v156, v150, v151, v160
	v_cmp_ge_i32_e32 vcc, v156, v157
	s_waitcnt vmcnt(5)
	v_mfma_f32_16x16x32_f16 v[136:139], v[96:99], v[112:115], 0
	v_mfma_f32_16x16x32_f16 v[140:143], v[100:103], v[112:115], 0
	v_cndmask_b32_e32 v158, 3, v158, vcc
	v_mfma_f32_16x16x32_f16 v[144:147], v[104:107], v[112:115], 0
	v_mfma_f32_16x16x32_f16 v[148:151], v[108:111], v[112:115], 0
	v_min3_i32 v160, v120, v121, v156
	v_min3_i32 v160, v122, v123, v160
	v_min3_i32 v160, v124, v125, v160
	v_min3_i32 v160, v126, v127, v160
	v_min3_i32 v160, v128, v129, v160
	v_min3_i32 v160, v130, v131, v160
	v_min3_i32 v160, v132, v133, v160
	v_min3_i32 v157, v134, v135, v160
	v_cmp_ge_i32_e32 vcc, v157, v156
	s_waitcnt vmcnt(4)
	global_load_dwordx4 v[112:115], v164, s[4:5] offset:2048
	v_mfma_f32_16x16x32_f16 v[120:123], v[16:19], v[116:119], 0
	v_mfma_f32_16x16x32_f16 v[124:127], v[20:23], v[116:119], 0
	v_cndmask_b32_e32 v158, 4, v158, vcc
	v_mfma_f32_16x16x32_f16 v[128:131], v[24:27], v[116:119], 0
	v_mfma_f32_16x16x32_f16 v[132:135], v[28:31], v[116:119], 0
	v_min3_i32 v160, v136, v137, v157
	v_min3_i32 v160, v138, v139, v160
	v_min3_i32 v160, v140, v141, v160
	v_min3_i32 v160, v142, v143, v160
	v_min3_i32 v160, v144, v145, v160
	v_min3_i32 v160, v146, v147, v160
	v_min3_i32 v160, v148, v149, v160
	v_min3_i32 v156, v150, v151, v160
	v_cmp_ge_i32_e32 vcc, v156, v157
	v_mfma_f32_16x16x32_f16 v[136:139], v[32:35], v[116:119], 0
	v_mfma_f32_16x16x32_f16 v[140:143], v[36:39], v[116:119], 0
	v_cndmask_b32_e32 v158, 5, v158, vcc
	v_add_u32_e32 v162, s40, v158
	v_lshl_or_b32 v162, v162, 2, v166
	v_mov_b32_e32 v163, v156
	ds_min_u64 v167, v[162:163] offset:16384
	v_mfma_f32_16x16x32_f16 v[144:147], v[40:43], v[116:119], 0
	v_mfma_f32_16x16x32_f16 v[148:151], v[44:47], v[116:119], 0
	v_min3_i32 v160, v120, v121, s41
	v_min3_i32 v160, v122, v123, v160
	v_min3_i32 v160, v124, v125, v160
	v_min3_i32 v160, v126, v127, v160
	v_min3_i32 v160, v128, v129, v160
	v_min3_i32 v160, v130, v131, v160
	v_min3_i32 v160, v132, v133, v160
	v_min3_i32 v157, v134, v135, v160
	v_mfma_f32_16x16x32_f16 v[120:123], v[48:51], v[116:119], 0
	v_mfma_f32_16x16x32_f16 v[124:127], v[52:55], v[116:119], 0
	v_mov_b32_e32 v158, 0
	v_mfma_f32_16x16x32_f16 v[128:131], v[56:59], v[116:119], 0
	v_mfma_f32_16x16x32_f16 v[132:135], v[60:63], v[116:119], 0
	v_min3_i32 v160, v136, v137, v157
	v_min3_i32 v160, v138, v139, v160
	v_min3_i32 v160, v140, v141, v160
	v_min3_i32 v160, v142, v143, v160
	v_min3_i32 v160, v144, v145, v160
	v_min3_i32 v160, v146, v147, v160
	v_min3_i32 v160, v148, v149, v160
	v_min3_i32 v156, v150, v151, v160
	v_cmp_ge_i32_e32 vcc, v156, v157
	v_mfma_f32_16x16x32_f16 v[136:139], v[64:67], v[116:119], 0
	v_mfma_f32_16x16x32_f16 v[140:143], v[68:71], v[116:119], 0
	v_cndmask_b32_e32 v158, 1, v158, vcc
	v_mfma_f32_16x16x32_f16 v[144:147], v[72:75], v[116:119], 0
	v_mfma_f32_16x16x32_f16 v[148:151], v[76:79], v[116:119], 0
	v_min3_i32 v160, v120, v121, v156
	v_min3_i32 v160, v122, v123, v160
	v_min3_i32 v160, v124, v125, v160
	v_min3_i32 v160, v126, v127, v160
	v_min3_i32 v160, v128, v129, v160
	v_min3_i32 v160, v130, v131, v160
	v_min3_i32 v160, v132, v133, v160
	v_min3_i32 v157, v134, v135, v160
	v_cmp_ge_i32_e32 vcc, v157, v156
	v_mfma_f32_16x16x32_f16 v[120:123], v[80:83], v[116:119], 0
	v_mfma_f32_16x16x32_f16 v[124:127], v[84:87], v[116:119], 0
	v_cndmask_b32_e32 v158, 2, v158, vcc
	v_mfma_f32_16x16x32_f16 v[128:131], v[88:91], v[116:119], 0
	v_mfma_f32_16x16x32_f16 v[132:135], v[92:95], v[116:119], 0
	v_min3_i32 v160, v136, v137, v157
	v_min3_i32 v160, v138, v139, v160
	v_min3_i32 v160, v140, v141, v160
	v_min3_i32 v160, v142, v143, v160
	v_min3_i32 v160, v144, v145, v160
	v_min3_i32 v160, v146, v147, v160
	v_min3_i32 v160, v148, v149, v160
	v_min3_i32 v156, v150, v151, v160
	v_cmp_ge_i32_e32 vcc, v156, v157
	v_mfma_f32_16x16x32_f16 v[136:139], v[96:99], v[116:119], 0
	v_mfma_f32_16x16x32_f16 v[140:143], v[100:103], v[116:119], 0
	v_cndmask_b32_e32 v158, 3, v158, vcc
	v_mfma_f32_16x16x32_f16 v[144:147], v[104:107], v[116:119], 0
	v_mfma_f32_16x16x32_f16 v[148:151], v[108:111], v[116:119], 0
	v_min3_i32 v160, v120, v121, v156
	v_min3_i32 v160, v122, v123, v160
	v_min3_i32 v160, v124, v125, v160
	v_min3_i32 v160, v126, v127, v160
	v_min3_i32 v160, v128, v129, v160
	v_min3_i32 v160, v130, v131, v160
	v_min3_i32 v160, v132, v133, v160
	v_min3_i32 v157, v134, v135, v160
	v_cmp_ge_i32_e32 vcc, v157, v156
	s_waitcnt vmcnt(0)
	global_load_dwordx4 v[116:119], v164, s[4:5] offset:3072
	v_mfma_f32_16x16x32_f16 v[120:123], v[16:19], v[112:115], 0
	v_mfma_f32_16x16x32_f16 v[124:127], v[20:23], v[112:115], 0
	v_cndmask_b32_e32 v158, 4, v158, vcc
	v_mfma_f32_16x16x32_f16 v[128:131], v[24:27], v[112:115], 0
	v_mfma_f32_16x16x32_f16 v[132:135], v[28:31], v[112:115], 0
	v_min3_i32 v160, v136, v137, v157
	v_min3_i32 v160, v138, v139, v160
	v_min3_i32 v160, v140, v141, v160
	v_min3_i32 v160, v142, v143, v160
	v_min3_i32 v160, v144, v145, v160
	v_min3_i32 v160, v146, v147, v160
	v_min3_i32 v160, v148, v149, v160
	v_min3_i32 v156, v150, v151, v160
	v_cmp_ge_i32_e32 vcc, v156, v157
	v_mfma_f32_16x16x32_f16 v[136:139], v[32:35], v[112:115], 0
	v_mfma_f32_16x16x32_f16 v[140:143], v[36:39], v[112:115], 0
	v_cndmask_b32_e32 v158, 5, v158, vcc
	v_add_u32_e32 v162, s40, v158
	v_lshl_or_b32 v162, v162, 2, v166
	v_mov_b32_e32 v163, v156
	ds_min_u64 v167, v[162:163] offset:16512
	v_mfma_f32_16x16x32_f16 v[144:147], v[40:43], v[112:115], 0
	v_mfma_f32_16x16x32_f16 v[148:151], v[44:47], v[112:115], 0
	v_min3_i32 v160, v120, v121, s41
	v_min3_i32 v160, v122, v123, v160
	v_min3_i32 v160, v124, v125, v160
	v_min3_i32 v160, v126, v127, v160
	v_min3_i32 v160, v128, v129, v160
	v_min3_i32 v160, v130, v131, v160
	v_min3_i32 v160, v132, v133, v160
	v_min3_i32 v157, v134, v135, v160
	v_mfma_f32_16x16x32_f16 v[120:123], v[48:51], v[112:115], 0
	v_mfma_f32_16x16x32_f16 v[124:127], v[52:55], v[112:115], 0
	v_mov_b32_e32 v158, 0
	v_mfma_f32_16x16x32_f16 v[128:131], v[56:59], v[112:115], 0
	v_mfma_f32_16x16x32_f16 v[132:135], v[60:63], v[112:115], 0
	v_min3_i32 v160, v136, v137, v157
	v_min3_i32 v160, v138, v139, v160
	v_min3_i32 v160, v140, v141, v160
	v_min3_i32 v160, v142, v143, v160
	v_min3_i32 v160, v144, v145, v160
	v_min3_i32 v160, v146, v147, v160
	v_min3_i32 v160, v148, v149, v160
	v_min3_i32 v156, v150, v151, v160
	v_cmp_ge_i32_e32 vcc, v156, v157
	v_mfma_f32_16x16x32_f16 v[136:139], v[64:67], v[112:115], 0
	v_mfma_f32_16x16x32_f16 v[140:143], v[68:71], v[112:115], 0
	v_cndmask_b32_e32 v158, 1, v158, vcc
	v_mfma_f32_16x16x32_f16 v[144:147], v[72:75], v[112:115], 0
	v_mfma_f32_16x16x32_f16 v[148:151], v[76:79], v[112:115], 0
	v_min3_i32 v160, v120, v121, v156
	v_min3_i32 v160, v122, v123, v160
	v_min3_i32 v160, v124, v125, v160
	v_min3_i32 v160, v126, v127, v160
	v_min3_i32 v160, v128, v129, v160
	v_min3_i32 v160, v130, v131, v160
	v_min3_i32 v160, v132, v133, v160
	v_min3_i32 v157, v134, v135, v160
	v_cmp_ge_i32_e32 vcc, v157, v156
	v_mfma_f32_16x16x32_f16 v[120:123], v[80:83], v[112:115], 0
	v_mfma_f32_16x16x32_f16 v[124:127], v[84:87], v[112:115], 0
	v_cndmask_b32_e32 v158, 2, v158, vcc
	v_mfma_f32_16x16x32_f16 v[128:131], v[88:91], v[112:115], 0
	v_mfma_f32_16x16x32_f16 v[132:135], v[92:95], v[112:115], 0
	v_min3_i32 v160, v136, v137, v157
	v_min3_i32 v160, v138, v139, v160
	v_min3_i32 v160, v140, v141, v160
	v_min3_i32 v160, v142, v143, v160
	v_min3_i32 v160, v144, v145, v160
	v_min3_i32 v160, v146, v147, v160
	v_min3_i32 v160, v148, v149, v160
	v_min3_i32 v156, v150, v151, v160
	v_cmp_ge_i32_e32 vcc, v156, v157
	v_mfma_f32_16x16x32_f16 v[136:139], v[96:99], v[112:115], 0
	v_mfma_f32_16x16x32_f16 v[140:143], v[100:103], v[112:115], 0
	v_cndmask_b32_e32 v158, 3, v158, vcc
	v_mfma_f32_16x16x32_f16 v[144:147], v[104:107], v[112:115], 0
	v_mfma_f32_16x16x32_f16 v[148:151], v[108:111], v[112:115], 0
	v_min3_i32 v160, v120, v121, v156
	v_min3_i32 v160, v122, v123, v160
	v_min3_i32 v160, v124, v125, v160
	v_min3_i32 v160, v126, v127, v160
	v_min3_i32 v160, v128, v129, v160
	v_min3_i32 v160, v130, v131, v160
	v_min3_i32 v160, v132, v133, v160
	v_min3_i32 v157, v134, v135, v160
	v_cmp_ge_i32_e32 vcc, v157, v156
	s_waitcnt vmcnt(0)
	global_load_dwordx4 v[112:115], v164, s[22:23]
	v_mfma_f32_16x16x32_f16 v[120:123], v[16:19], v[116:119], 0
	v_mfma_f32_16x16x32_f16 v[124:127], v[20:23], v[116:119], 0
	v_cndmask_b32_e32 v158, 4, v158, vcc
	v_mfma_f32_16x16x32_f16 v[128:131], v[24:27], v[116:119], 0
	v_mfma_f32_16x16x32_f16 v[132:135], v[28:31], v[116:119], 0
	v_min3_i32 v160, v136, v137, v157
	v_min3_i32 v160, v138, v139, v160
	v_min3_i32 v160, v140, v141, v160
	v_min3_i32 v160, v142, v143, v160
	v_min3_i32 v160, v144, v145, v160
	v_min3_i32 v160, v146, v147, v160
	v_min3_i32 v160, v148, v149, v160
	v_min3_i32 v156, v150, v151, v160
	v_cmp_ge_i32_e32 vcc, v156, v157
	v_mfma_f32_16x16x32_f16 v[136:139], v[32:35], v[116:119], 0
	v_mfma_f32_16x16x32_f16 v[140:143], v[36:39], v[116:119], 0
	v_cndmask_b32_e32 v158, 5, v158, vcc
	v_add_u32_e32 v162, s40, v158
	v_lshl_or_b32 v162, v162, 2, v166
	v_mov_b32_e32 v163, v156
	ds_min_u64 v167, v[162:163] offset:16640
	v_mfma_f32_16x16x32_f16 v[144:147], v[40:43], v[116:119], 0
	v_mfma_f32_16x16x32_f16 v[148:151], v[44:47], v[116:119], 0
	v_min3_i32 v160, v120, v121, s41
	v_min3_i32 v160, v122, v123, v160
	v_min3_i32 v160, v124, v125, v160
	v_min3_i32 v160, v126, v127, v160
	v_min3_i32 v160, v128, v129, v160
	v_min3_i32 v160, v130, v131, v160
	v_min3_i32 v160, v132, v133, v160
	v_min3_i32 v157, v134, v135, v160
	v_mfma_f32_16x16x32_f16 v[120:123], v[48:51], v[116:119], 0
	v_mfma_f32_16x16x32_f16 v[124:127], v[52:55], v[116:119], 0
	v_mov_b32_e32 v158, 0
	v_mfma_f32_16x16x32_f16 v[128:131], v[56:59], v[116:119], 0
	v_mfma_f32_16x16x32_f16 v[132:135], v[60:63], v[116:119], 0
	v_min3_i32 v160, v136, v137, v157
	v_min3_i32 v160, v138, v139, v160
	v_min3_i32 v160, v140, v141, v160
	v_min3_i32 v160, v142, v143, v160
	v_min3_i32 v160, v144, v145, v160
	v_min3_i32 v160, v146, v147, v160
	v_min3_i32 v160, v148, v149, v160
	v_min3_i32 v156, v150, v151, v160
	v_cmp_ge_i32_e32 vcc, v156, v157
	v_mfma_f32_16x16x32_f16 v[136:139], v[64:67], v[116:119], 0
	v_mfma_f32_16x16x32_f16 v[140:143], v[68:71], v[116:119], 0
	v_cndmask_b32_e32 v158, 1, v158, vcc
	v_mfma_f32_16x16x32_f16 v[144:147], v[72:75], v[116:119], 0
	v_mfma_f32_16x16x32_f16 v[148:151], v[76:79], v[116:119], 0
	v_min3_i32 v160, v120, v121, v156
	v_min3_i32 v160, v122, v123, v160
	v_min3_i32 v160, v124, v125, v160
	v_min3_i32 v160, v126, v127, v160
	v_min3_i32 v160, v128, v129, v160
	v_min3_i32 v160, v130, v131, v160
	v_min3_i32 v160, v132, v133, v160
	v_min3_i32 v157, v134, v135, v160
	v_cmp_ge_i32_e32 vcc, v157, v156
	s_waitcnt lgkmcnt(0)
	s_barrier
	s_cmp_lt_u32 s50, 3
	s_cbranch_scc0 .Lp1a_3_x
	s_lshl_b32 s60, s50, 7
	v_add_u32_e32 v2, s60, v169
	ds_read_b32 v178, v2 offset:16384
	s_lshl_b32 s60, s50, 10
	v_add_u32_e32 v210, s60, v170
.Lp1a_3_x:
	v_mfma_f32_16x16x32_f16 v[120:123], v[80:83], v[116:119], 0
	v_mfma_f32_16x16x32_f16 v[124:127], v[84:87], v[116:119], 0
	v_cndmask_b32_e32 v158, 2, v158, vcc
	v_mfma_f32_16x16x32_f16 v[128:131], v[88:91], v[116:119], 0
	v_mfma_f32_16x16x32_f16 v[132:135], v[92:95], v[116:119], 0
	v_min3_i32 v160, v136, v137, v157
	v_min3_i32 v160, v138, v139, v160
	v_min3_i32 v160, v140, v141, v160
	v_min3_i32 v160, v142, v143, v160
	v_min3_i32 v160, v144, v145, v160
	v_min3_i32 v160, v146, v147, v160
	v_min3_i32 v160, v148, v149, v160
	v_min3_i32 v156, v150, v151, v160
	v_cmp_ge_i32_e32 vcc, v156, v157
	s_waitcnt lgkmcnt(0)
	s_cmp_lt_u32 s50, 3
	s_cbranch_scc0 .Lp1b_3_x
	v_lshrrev_b32_e32 v2, 2, v178
	v_mul_u32_u24_e32 v3, 43, v2
	v_lshrrev_b32_e32 v3, 8, v3
	v_mul_u32_u24_e32 v4, 6, v3
	v_sub_u32_e32 v4, v2, v4
	v_mul_u32_u24_e32 v3, 24, v3
	v_min_u32_e32 v3, 0xa5, v3
	v_lshl_add_u32 v3, v4, 2, v3
	v_lshrrev_b32_e32 v4, 2, v168
	v_add_u32_e32 v3, v3, v4
	v_and_b32_e32 v4, 3, v178
	v_lshlrev_b32_e32 v4, 2, v4
	v_and_b32_e32 v5, 3, v168
	v_or_b32_e32 v4, v4, v5
	v_lshl_or_b32 v214, v3, 4, v4
	v_add_u32_e32 v3, s9, v3
	v_lshlrev_b32_e32 v4, 4, v4
	v_lshl_or_b32 v206, v3, 10, v4
	global_load_dwordx4 v[178:181], v206, s[6:7]
	global_load_dwordx4 v[182:185], v206, s[6:7] offset:256
	global_load_dwordx4 v[186:189], v206, s[6:7] offset:512
	global_load_dwordx4 v[190:193], v206, s[6:7] offset:768
	global_load_dwordx4 v[194:197], v206, s[6:7] offset:2048
	global_load_dwordx4 v[198:201], v206, s[6:7] offset:2304
	global_load_dwordx4 v[202:205], v206, s[6:7] offset:2560
	global_load_dwordx4 v[206:209], v206, s[6:7] offset:2816
	global_load_dwordx4 v[210:213], v210, s[4:5]
.Lp1b_3_x:
	v_mfma_f32_16x16x32_f16 v[136:139], v[96:99], v[116:119], 0
	v_mfma_f32_16x16x32_f16 v[140:143], v[100:103], v[116:119], 0
	v_cndmask_b32_e32 v158, 3, v158, vcc
	v_mfma_f32_16x16x32_f16 v[144:147], v[104:107], v[116:119], 0
	v_mfma_f32_16x16x32_f16 v[148:151], v[108:111], v[116:119], 0
	v_min3_i32 v160, v120, v121, v156
	v_min3_i32 v160, v122, v123, v160
	v_min3_i32 v160, v124, v125, v160
	v_min3_i32 v160, v126, v127, v160
	v_min3_i32 v160, v128, v129, v160
	v_min3_i32 v160, v130, v131, v160
	v_min3_i32 v160, v132, v133, v160
	v_min3_i32 v157, v134, v135, v160
	v_cmp_ge_i32_e32 vcc, v157, v156
	s_cmp_lt_u32 s50, 3
	s_cbranch_scc1 .Lit4a
	s_waitcnt vmcnt(0)
	s_branch .Lit4b

.Lit4b:
	global_load_dwordx4 v[116:119], v164, s[22:23] offset:1024
	v_mfma_f32_16x16x32_f16 v[120:123], v[16:19], v[112:115], 0
	v_mfma_f32_16x16x32_f16 v[124:127], v[20:23], v[112:115], 0
	v_cndmask_b32_e32 v158, 4, v158, vcc
	v_mfma_f32_16x16x32_f16 v[128:131], v[24:27], v[112:115], 0
	v_mfma_f32_16x16x32_f16 v[132:135], v[28:31], v[112:115], 0
	v_min3_i32 v160, v136, v137, v157
	v_min3_i32 v160, v138, v139, v160
	v_min3_i32 v160, v140, v141, v160
	v_min3_i32 v160, v142, v143, v160
	v_min3_i32 v160, v144, v145, v160
	v_min3_i32 v160, v146, v147, v160
	v_min3_i32 v160, v148, v149, v160
	v_min3_i32 v156, v150, v151, v160
	v_cmp_ge_i32_e32 vcc, v156, v157
	v_mfma_f32_16x16x32_f16 v[136:139], v[32:35], v[112:115], 0
	v_mfma_f32_16x16x32_f16 v[140:143], v[36:39], v[112:115], 0
	v_cndmask_b32_e32 v158, 5, v158, vcc
	v_add_u32_e32 v162, s40, v158
	v_lshl_or_b32 v162, v162, 2, v166
	v_mov_b32_e32 v163, v156
	ds_min_u64 v167, v[162:163] offset:16768
	v_mfma_f32_16x16x32_f16 v[144:147], v[40:43], v[112:115], 0
	v_mfma_f32_16x16x32_f16 v[148:151], v[44:47], v[112:115], 0
	v_min3_i32 v160, v120, v121, s41
	v_min3_i32 v160, v122, v123, v160
	v_min3_i32 v160, v124, v125, v160
	v_min3_i32 v160, v126, v127, v160
	v_min3_i32 v160, v128, v129, v160
	v_min3_i32 v160, v130, v131, v160
	v_min3_i32 v160, v132, v133, v160
	v_min3_i32 v157, v134, v135, v160
	v_mfma_f32_16x16x32_f16 v[120:123], v[48:51], v[112:115], 0
	v_mfma_f32_16x16x32_f16 v[124:127], v[52:55], v[112:115], 0
	v_mov_b32_e32 v158, 0
	v_mfma_f32_16x16x32_f16 v[128:131], v[56:59], v[112:115], 0
	v_mfma_f32_16x16x32_f16 v[132:135], v[60:63], v[112:115], 0
	v_min3_i32 v160, v136, v137, v157
	v_min3_i32 v160, v138, v139, v160
	v_min3_i32 v160, v140, v141, v160
	v_min3_i32 v160, v142, v143, v160
	v_min3_i32 v160, v144, v145, v160
	v_min3_i32 v160, v146, v147, v160
	v_min3_i32 v160, v148, v149, v160
	v_min3_i32 v156, v150, v151, v160
	v_cmp_ge_i32_e32 vcc, v156, v157
	v_mfma_f32_16x16x32_f16 v[136:139], v[64:67], v[112:115], 0
	v_mfma_f32_16x16x32_f16 v[140:143], v[68:71], v[112:115], 0
	v_cndmask_b32_e32 v158, 1, v158, vcc
	v_mfma_f32_16x16x32_f16 v[144:147], v[72:75], v[112:115], 0
	v_mfma_f32_16x16x32_f16 v[148:151], v[76:79], v[112:115], 0
	v_min3_i32 v160, v120, v121, v156
	v_min3_i32 v160, v122, v123, v160
	v_min3_i32 v160, v124, v125, v160
	v_min3_i32 v160, v126, v127, v160
	v_min3_i32 v160, v128, v129, v160
	v_min3_i32 v160, v130, v131, v160
	v_min3_i32 v160, v132, v133, v160
	v_min3_i32 v157, v134, v135, v160
	v_cmp_ge_i32_e32 vcc, v157, v156
	v_mfma_f32_16x16x32_f16 v[120:123], v[80:83], v[112:115], 0
	v_mfma_f32_16x16x32_f16 v[124:127], v[84:87], v[112:115], 0
	v_cndmask_b32_e32 v158, 2, v158, vcc
	v_mfma_f32_16x16x32_f16 v[128:131], v[88:91], v[112:115], 0
	v_mfma_f32_16x16x32_f16 v[132:135], v[92:95], v[112:115], 0
	v_min3_i32 v160, v136, v137, v157
	v_min3_i32 v160, v138, v139, v160
	v_min3_i32 v160, v140, v141, v160
	v_min3_i32 v160, v142, v143, v160
	v_min3_i32 v160, v144, v145, v160
	v_min3_i32 v160, v146, v147, v160
	v_min3_i32 v160, v148, v149, v160
	v_min3_i32 v156, v150, v151, v160
	v_cmp_ge_i32_e32 vcc, v156, v157
	v_mfma_f32_16x16x32_f16 v[136:139], v[96:99], v[112:115], 0
	v_mfma_f32_16x16x32_f16 v[140:143], v[100:103], v[112:115], 0
	v_cndmask_b32_e32 v158, 3, v158, vcc
	v_mfma_f32_16x16x32_f16 v[144:147], v[104:107], v[112:115], 0
	v_mfma_f32_16x16x32_f16 v[148:151], v[108:111], v[112:115], 0
	v_min3_i32 v160, v120, v121, v156
	v_min3_i32 v160, v122, v123, v160
	v_min3_i32 v160, v124, v125, v160
	v_min3_i32 v160, v126, v127, v160
	v_min3_i32 v160, v128, v129, v160
	v_min3_i32 v160, v130, v131, v160
	v_min3_i32 v160, v132, v133, v160
	v_min3_i32 v157, v134, v135, v160
	v_cmp_ge_i32_e32 vcc, v157, v156
	s_waitcnt vmcnt(0)
	global_load_dwordx4 v[112:115], v164, s[22:23] offset:2048
	v_mfma_f32_16x16x32_f16 v[120:123], v[16:19], v[116:119], 0
	v_mfma_f32_16x16x32_f16 v[124:127], v[20:23], v[116:119], 0
	v_cndmask_b32_e32 v158, 4, v158, vcc
	v_mfma_f32_16x16x32_f16 v[128:131], v[24:27], v[116:119], 0
	v_mfma_f32_16x16x32_f16 v[132:135], v[28:31], v[116:119], 0
	v_min3_i32 v160, v136, v137, v157
	v_min3_i32 v160, v138, v139, v160
	v_min3_i32 v160, v140, v141, v160
	v_min3_i32 v160, v142, v143, v160
	v_min3_i32 v160, v144, v145, v160
	v_min3_i32 v160, v146, v147, v160
	v_min3_i32 v160, v148, v149, v160
	v_min3_i32 v156, v150, v151, v160
	v_cmp_ge_i32_e32 vcc, v156, v157
	v_mfma_f32_16x16x32_f16 v[136:139], v[32:35], v[116:119], 0
	v_mfma_f32_16x16x32_f16 v[140:143], v[36:39], v[116:119], 0
	v_cndmask_b32_e32 v158, 5, v158, vcc
	v_add_u32_e32 v162, s40, v158
	v_lshl_or_b32 v162, v162, 2, v166
	v_mov_b32_e32 v163, v156
	ds_min_u64 v167, v[162:163] offset:16896
	v_mfma_f32_16x16x32_f16 v[144:147], v[40:43], v[116:119], 0
	v_mfma_f32_16x16x32_f16 v[148:151], v[44:47], v[116:119], 0
	v_min3_i32 v160, v120, v121, s41
	v_min3_i32 v160, v122, v123, v160
	v_min3_i32 v160, v124, v125, v160
	v_min3_i32 v160, v126, v127, v160
	v_min3_i32 v160, v128, v129, v160
	v_min3_i32 v160, v130, v131, v160
	v_min3_i32 v160, v132, v133, v160
	v_min3_i32 v157, v134, v135, v160
	v_mfma_f32_16x16x32_f16 v[120:123], v[48:51], v[116:119], 0
	v_mfma_f32_16x16x32_f16 v[124:127], v[52:55], v[116:119], 0
	v_mov_b32_e32 v158, 0
	v_mfma_f32_16x16x32_f16 v[128:131], v[56:59], v[116:119], 0
	v_mfma_f32_16x16x32_f16 v[132:135], v[60:63], v[116:119], 0
	v_min3_i32 v160, v136, v137, v157
	v_min3_i32 v160, v138, v139, v160
	v_min3_i32 v160, v140, v141, v160
	v_min3_i32 v160, v142, v143, v160
	v_min3_i32 v160, v144, v145, v160
	v_min3_i32 v160, v146, v147, v160
	v_min3_i32 v160, v148, v149, v160
	v_min3_i32 v156, v150, v151, v160
	v_cmp_ge_i32_e32 vcc, v156, v157
	v_mfma_f32_16x16x32_f16 v[136:139], v[64:67], v[116:119], 0
	v_mfma_f32_16x16x32_f16 v[140:143], v[68:71], v[116:119], 0
	v_cndmask_b32_e32 v158, 1, v158, vcc
	v_mfma_f32_16x16x32_f16 v[144:147], v[72:75], v[116:119], 0
	v_mfma_f32_16x16x32_f16 v[148:151], v[76:79], v[116:119], 0
	v_min3_i32 v160, v120, v121, v156
	v_min3_i32 v160, v122, v123, v160
	v_min3_i32 v160, v124, v125, v160
	v_min3_i32 v160, v126, v127, v160
	v_min3_i32 v160, v128, v129, v160
	v_min3_i32 v160, v130, v131, v160
	v_min3_i32 v160, v132, v133, v160
	v_min3_i32 v157, v134, v135, v160
	v_cmp_ge_i32_e32 vcc, v157, v156
	v_mfma_f32_16x16x32_f16 v[120:123], v[80:83], v[116:119], 0
	v_mfma_f32_16x16x32_f16 v[124:127], v[84:87], v[116:119], 0
	v_cndmask_b32_e32 v158, 2, v158, vcc
	v_mfma_f32_16x16x32_f16 v[128:131], v[88:91], v[116:119], 0
	v_mfma_f32_16x16x32_f16 v[132:135], v[92:95], v[116:119], 0
	v_min3_i32 v160, v136, v137, v157
	v_min3_i32 v160, v138, v139, v160
	v_min3_i32 v160, v140, v141, v160
	v_min3_i32 v160, v142, v143, v160
	v_min3_i32 v160, v144, v145, v160
	v_min3_i32 v160, v146, v147, v160
	v_min3_i32 v160, v148, v149, v160
	v_min3_i32 v156, v150, v151, v160
	v_cmp_ge_i32_e32 vcc, v156, v157
	v_mfma_f32_16x16x32_f16 v[136:139], v[96:99], v[116:119], 0
	v_mfma_f32_16x16x32_f16 v[140:143], v[100:103], v[116:119], 0
	v_cndmask_b32_e32 v158, 3, v158, vcc
	v_mfma_f32_16x16x32_f16 v[144:147], v[104:107], v[116:119], 0
	v_mfma_f32_16x16x32_f16 v[148:151], v[108:111], v[116:119], 0
	v_min3_i32 v160, v120, v121, v156
	v_min3_i32 v160, v122, v123, v160
	v_min3_i32 v160, v124, v125, v160
	v_min3_i32 v160, v126, v127, v160
	v_min3_i32 v160, v128, v129, v160
	v_min3_i32 v160, v130, v131, v160
	v_min3_i32 v160, v132, v133, v160
	v_min3_i32 v157, v134, v135, v160
	v_cmp_ge_i32_e32 vcc, v157, v156
	s_waitcnt vmcnt(0)
	global_load_dwordx4 v[116:119], v164, s[22:23] offset:3072
	v_mfma_f32_16x16x32_f16 v[120:123], v[16:19], v[112:115], 0
	v_mfma_f32_16x16x32_f16 v[124:127], v[20:23], v[112:115], 0
	v_cndmask_b32_e32 v158, 4, v158, vcc
	v_mfma_f32_16x16x32_f16 v[128:131], v[24:27], v[112:115], 0
	v_mfma_f32_16x16x32_f16 v[132:135], v[28:31], v[112:115], 0
	v_min3_i32 v160, v136, v137, v157
	v_min3_i32 v160, v138, v139, v160
	v_min3_i32 v160, v140, v141, v160
	v_min3_i32 v160, v142, v143, v160
	v_min3_i32 v160, v144, v145, v160
	v_min3_i32 v160, v146, v147, v160
	v_min3_i32 v160, v148, v149, v160
	v_min3_i32 v156, v150, v151, v160
	v_cmp_ge_i32_e32 vcc, v156, v157
	v_mfma_f32_16x16x32_f16 v[136:139], v[32:35], v[112:115], 0
	v_mfma_f32_16x16x32_f16 v[140:143], v[36:39], v[112:115], 0
	v_cndmask_b32_e32 v158, 5, v158, vcc
	v_add_u32_e32 v162, s40, v158
	v_lshl_or_b32 v162, v162, 2, v166
	v_mov_b32_e32 v163, v156
	ds_min_u64 v167, v[162:163] offset:17024
	v_mfma_f32_16x16x32_f16 v[144:147], v[40:43], v[112:115], 0
	v_mfma_f32_16x16x32_f16 v[148:151], v[44:47], v[112:115], 0
	v_min3_i32 v160, v120, v121, s41
	v_min3_i32 v160, v122, v123, v160
	v_min3_i32 v160, v124, v125, v160
	v_min3_i32 v160, v126, v127, v160
	v_min3_i32 v160, v128, v129, v160
	v_min3_i32 v160, v130, v131, v160
	v_min3_i32 v160, v132, v133, v160
	v_min3_i32 v157, v134, v135, v160
	v_mfma_f32_16x16x32_f16 v[120:123], v[48:51], v[112:115], 0
	v_mfma_f32_16x16x32_f16 v[124:127], v[52:55], v[112:115], 0
	v_mov_b32_e32 v158, 0
	v_mfma_f32_16x16x32_f16 v[128:131], v[56:59], v[112:115], 0
	v_mfma_f32_16x16x32_f16 v[132:135], v[60:63], v[112:115], 0
	v_min3_i32 v160, v136, v137, v157
	v_min3_i32 v160, v138, v139, v160
	v_min3_i32 v160, v140, v141, v160
	v_min3_i32 v160, v142, v143, v160
	v_min3_i32 v160, v144, v145, v160
	v_min3_i32 v160, v146, v147, v160
	v_min3_i32 v160, v148, v149, v160
	v_min3_i32 v156, v150, v151, v160
	v_cmp_ge_i32_e32 vcc, v156, v157
	v_mfma_f32_16x16x32_f16 v[136:139], v[64:67], v[112:115], 0
	v_mfma_f32_16x16x32_f16 v[140:143], v[68:71], v[112:115], 0
	v_cndmask_b32_e32 v158, 1, v158, vcc
	v_mfma_f32_16x16x32_f16 v[144:147], v[72:75], v[112:115], 0
	v_mfma_f32_16x16x32_f16 v[148:151], v[76:79], v[112:115], 0
	v_min3_i32 v160, v120, v121, v156
	v_min3_i32 v160, v122, v123, v160
	v_min3_i32 v160, v124, v125, v160
	v_min3_i32 v160, v126, v127, v160
	v_min3_i32 v160, v128, v129, v160
	v_min3_i32 v160, v130, v131, v160
	v_min3_i32 v160, v132, v133, v160
	v_min3_i32 v157, v134, v135, v160
	v_cmp_ge_i32_e32 vcc, v157, v156
	s_waitcnt lgkmcnt(0)
	s_barrier
	s_cmp_eq_u32 s50, 3
	s_cbranch_scc0 .Lp1a_6_x
	s_lshl_b32 s60, s50, 7
	v_add_u32_e32 v2, s60, v169
	ds_read_b32 v178, v2 offset:16384
	s_lshl_b32 s60, s50, 10
	v_add_u32_e32 v210, s60, v170
.Lp1a_6_x:
	s_cmp_lt_u32 s50, 2
	s_cbranch_scc0 .Lp1a_6_y
	s_add_i32 s65, s50, 4
	s_lshl_b32 s60, s65, 7
	v_add_u32_e32 v2, s60, v169
	ds_read_b32 v216, v2 offset:16384
	s_lshl_b32 s60, s65, 10
	v_add_u32_e32 v248, s60, v170
.Lp1a_6_y:
	v_mfma_f32_16x16x32_f16 v[120:123], v[80:83], v[112:115], 0
	v_mfma_f32_16x16x32_f16 v[124:127], v[84:87], v[112:115], 0
	v_cndmask_b32_e32 v158, 2, v158, vcc
	v_mfma_f32_16x16x32_f16 v[128:131], v[88:91], v[112:115], 0
	v_mfma_f32_16x16x32_f16 v[132:135], v[92:95], v[112:115], 0
	v_min3_i32 v160, v136, v137, v157
	v_min3_i32 v160, v138, v139, v160
	v_min3_i32 v160, v140, v141, v160
	v_min3_i32 v160, v142, v143, v160
	v_min3_i32 v160, v144, v145, v160
	v_min3_i32 v160, v146, v147, v160
	v_min3_i32 v160, v148, v149, v160
	v_min3_i32 v156, v150, v151, v160
	v_cmp_ge_i32_e32 vcc, v156, v157
	s_waitcnt lgkmcnt(0)
	s_cmp_eq_u32 s50, 3
	s_cbranch_scc0 .Lp1b_6_x
	v_lshrrev_b32_e32 v2, 2, v178
	v_mul_u32_u24_e32 v3, 43, v2
	v_lshrrev_b32_e32 v3, 8, v3
	v_mul_u32_u24_e32 v4, 6, v3
	v_sub_u32_e32 v4, v2, v4
	v_mul_u32_u24_e32 v3, 24, v3
	v_min_u32_e32 v3, 0xa5, v3
	v_lshl_add_u32 v3, v4, 2, v3
	v_lshrrev_b32_e32 v4, 2, v168
	v_add_u32_e32 v3, v3, v4
	v_and_b32_e32 v4, 3, v178
	v_lshlrev_b32_e32 v4, 2, v4
	v_and_b32_e32 v5, 3, v168
	v_or_b32_e32 v4, v4, v5
	v_lshl_or_b32 v214, v3, 4, v4
	v_add_u32_e32 v3, s9, v3
	v_lshlrev_b32_e32 v4, 4, v4
	v_lshl_or_b32 v206, v3, 10, v4
	global_load_dwordx4 v[178:181], v206, s[6:7]
	global_load_dwordx4 v[182:185], v206, s[6:7] offset:256
	global_load_dwordx4 v[186:189], v206, s[6:7] offset:512
	global_load_dwordx4 v[190:193], v206, s[6:7] offset:768
	global_load_dwordx4 v[194:197], v206, s[6:7] offset:2048
	global_load_dwordx4 v[198:201], v206, s[6:7] offset:2304
	global_load_dwordx4 v[202:205], v206, s[6:7] offset:2560
	global_load_dwordx4 v[206:209], v206, s[6:7] offset:2816
	global_load_dwordx4 v[210:213], v210, s[4:5]

.Lp1b_6_y:
	v_mfma_f32_16x16x32_f16 v[136:139], v[96:99], v[112:115], 0
	v_mfma_f32_16x16x32_f16 v[140:143], v[100:103], v[112:115], 0
	v_cndmask_b32_e32 v158, 3, v158, vcc
	v_mfma_f32_16x16x32_f16 v[144:147], v[104:107], v[112:115], 0
	v_mfma_f32_16x16x32_f16 v[148:151], v[108:111], v[112:115], 0
	v_min3_i32 v160, v120, v121, v156
	v_min3_i32 v160, v122, v123, v160
	v_min3_i32 v160, v124, v125, v160
	v_min3_i32 v160, v126, v127, v160
	v_min3_i32 v160, v128, v129, v160
	v_min3_i32 v160, v130, v131, v160
	v_min3_i32 v160, v132, v133, v160
	v_min3_i32 v157, v134, v135, v160
	v_cmp_ge_i32_e32 vcc, v157, v156
	s_cmp_lg_u32 s50, 2
	s_cbranch_scc1 .Lit7a
	s_waitcnt vmcnt(0)
	s_branch .Lit7b

.Lit7b:
	global_load_dwordx4 v[112:115], v164, s[24:25]
	v_mfma_f32_16x16x32_f16 v[120:123], v[16:19], v[116:119], 0
	v_mfma_f32_16x16x32_f16 v[124:127], v[20:23], v[116:119], 0
	v_cndmask_b32_e32 v158, 4, v158, vcc
	v_mfma_f32_16x16x32_f16 v[128:131], v[24:27], v[116:119], 0
	v_mfma_f32_16x16x32_f16 v[132:135], v[28:31], v[116:119], 0
	v_min3_i32 v160, v136, v137, v157
	v_min3_i32 v160, v138, v139, v160
	v_min3_i32 v160, v140, v141, v160
	v_min3_i32 v160, v142, v143, v160
	v_min3_i32 v160, v144, v145, v160
	v_min3_i32 v160, v146, v147, v160
	v_min3_i32 v160, v148, v149, v160
	v_min3_i32 v156, v150, v151, v160
	v_cmp_ge_i32_e32 vcc, v156, v157
	v_mfma_f32_16x16x32_f16 v[136:139], v[32:35], v[116:119], 0
	v_mfma_f32_16x16x32_f16 v[140:143], v[36:39], v[116:119], 0
	v_cndmask_b32_e32 v158, 5, v158, vcc
	v_add_u32_e32 v162, s40, v158
	v_lshl_or_b32 v162, v162, 2, v166
	v_mov_b32_e32 v163, v156
	ds_min_u64 v167, v[162:163] offset:17152
	v_mfma_f32_16x16x32_f16 v[144:147], v[40:43], v[116:119], 0
	v_mfma_f32_16x16x32_f16 v[148:151], v[44:47], v[116:119], 0
	v_min3_i32 v160, v120, v121, s41
	v_min3_i32 v160, v122, v123, v160
	v_min3_i32 v160, v124, v125, v160
	v_min3_i32 v160, v126, v127, v160
	v_min3_i32 v160, v128, v129, v160
	v_min3_i32 v160, v130, v131, v160
	v_min3_i32 v160, v132, v133, v160
	v_min3_i32 v157, v134, v135, v160
	v_mfma_f32_16x16x32_f16 v[120:123], v[48:51], v[116:119], 0
	v_mfma_f32_16x16x32_f16 v[124:127], v[52:55], v[116:119], 0
	v_mov_b32_e32 v158, 0
	v_mfma_f32_16x16x32_f16 v[128:131], v[56:59], v[116:119], 0
	v_mfma_f32_16x16x32_f16 v[132:135], v[60:63], v[116:119], 0
	v_min3_i32 v160, v136, v137, v157
	v_min3_i32 v160, v138, v139, v160
	v_min3_i32 v160, v140, v141, v160
	v_min3_i32 v160, v142, v143, v160
	v_min3_i32 v160, v144, v145, v160
	v_min3_i32 v160, v146, v147, v160
	v_min3_i32 v160, v148, v149, v160
	v_min3_i32 v156, v150, v151, v160
	v_cmp_ge_i32_e32 vcc, v156, v157
	v_mfma_f32_16x16x32_f16 v[136:139], v[64:67], v[116:119], 0
	v_mfma_f32_16x16x32_f16 v[140:143], v[68:71], v[116:119], 0
	v_cndmask_b32_e32 v158, 1, v158, vcc
	v_mfma_f32_16x16x32_f16 v[144:147], v[72:75], v[116:119], 0
	v_mfma_f32_16x16x32_f16 v[148:151], v[76:79], v[116:119], 0
	v_min3_i32 v160, v120, v121, v156
	v_min3_i32 v160, v122, v123, v160
	v_min3_i32 v160, v124, v125, v160
	v_min3_i32 v160, v126, v127, v160
	v_min3_i32 v160, v128, v129, v160
	v_min3_i32 v160, v130, v131, v160
	v_min3_i32 v160, v132, v133, v160
	v_min3_i32 v157, v134, v135, v160
	v_cmp_ge_i32_e32 vcc, v157, v156
	v_mfma_f32_16x16x32_f16 v[120:123], v[80:83], v[116:119], 0
	v_mfma_f32_16x16x32_f16 v[124:127], v[84:87], v[116:119], 0
	v_cndmask_b32_e32 v158, 2, v158, vcc
	v_mfma_f32_16x16x32_f16 v[128:131], v[88:91], v[116:119], 0
	v_mfma_f32_16x16x32_f16 v[132:135], v[92:95], v[116:119], 0
	v_min3_i32 v160, v136, v137, v157
	v_min3_i32 v160, v138, v139, v160
	v_min3_i32 v160, v140, v141, v160
	v_min3_i32 v160, v142, v143, v160
	v_min3_i32 v160, v144, v145, v160
	v_min3_i32 v160, v146, v147, v160
	v_min3_i32 v160, v148, v149, v160
	v_min3_i32 v156, v150, v151, v160
	v_cmp_ge_i32_e32 vcc, v156, v157
	v_mfma_f32_16x16x32_f16 v[136:139], v[96:99], v[116:119], 0
	v_mfma_f32_16x16x32_f16 v[140:143], v[100:103], v[116:119], 0
	v_cndmask_b32_e32 v158, 3, v158, vcc
	v_mfma_f32_16x16x32_f16 v[144:147], v[104:107], v[116:119], 0
	v_mfma_f32_16x16x32_f16 v[148:151], v[108:111], v[116:119], 0
	v_min3_i32 v160, v120, v121, v156
	v_min3_i32 v160, v122, v123, v160
	v_min3_i32 v160, v124, v125, v160
	v_min3_i32 v160, v126, v127, v160
	v_min3_i32 v160, v128, v129, v160
	v_min3_i32 v160, v130, v131, v160
	v_min3_i32 v160, v132, v133, v160
	v_min3_i32 v157, v134, v135, v160
	v_cmp_ge_i32_e32 vcc, v157, v156
	s_waitcnt vmcnt(0)
	v_mfma_f32_16x16x32_f16 v[120:123], v[16:19], v[112:115], 0
	v_mfma_f32_16x16x32_f16 v[124:127], v[20:23], v[112:115], 0
	v_cndmask_b32_e32 v158, 4, v158, vcc
	v_mfma_f32_16x16x32_f16 v[128:131], v[24:27], v[112:115], 0
	v_mfma_f32_16x16x32_f16 v[132:135], v[28:31], v[112:115], 0
	v_min3_i32 v160, v136, v137, v157
	v_min3_i32 v160, v138, v139, v160
	v_min3_i32 v160, v140, v141, v160
	v_min3_i32 v160, v142, v143, v160
	v_min3_i32 v160, v144, v145, v160
	v_min3_i32 v160, v146, v147, v160
	v_min3_i32 v160, v148, v149, v160
	v_min3_i32 v156, v150, v151, v160
	v_cmp_ge_i32_e32 vcc, v156, v157
	v_mfma_f32_16x16x32_f16 v[136:139], v[32:35], v[112:115], 0
	v_mfma_f32_16x16x32_f16 v[140:143], v[36:39], v[112:115], 0
	v_cndmask_b32_e32 v158, 5, v158, vcc
	v_add_u32_e32 v162, s40, v158
	v_lshl_or_b32 v162, v162, 2, v166
	v_mov_b32_e32 v163, v156
	ds_min_u64 v167, v[162:163] offset:17280
	v_mfma_f32_16x16x32_f16 v[144:147], v[40:43], v[112:115], 0
	v_mfma_f32_16x16x32_f16 v[148:151], v[44:47], v[112:115], 0
	v_min3_i32 v160, v120, v121, s41
	v_min3_i32 v160, v122, v123, v160
	v_min3_i32 v160, v124, v125, v160
	v_min3_i32 v160, v126, v127, v160
	v_min3_i32 v160, v128, v129, v160
	v_min3_i32 v160, v130, v131, v160
	v_min3_i32 v160, v132, v133, v160
	v_min3_i32 v157, v134, v135, v160
	v_mfma_f32_16x16x32_f16 v[120:123], v[48:51], v[112:115], 0
	v_mfma_f32_16x16x32_f16 v[124:127], v[52:55], v[112:115], 0
	v_mov_b32_e32 v158, 0
	v_mfma_f32_16x16x32_f16 v[128:131], v[56:59], v[112:115], 0
	v_mfma_f32_16x16x32_f16 v[132:135], v[60:63], v[112:115], 0
	v_min3_i32 v160, v136, v137, v157
	v_min3_i32 v160, v138, v139, v160
	v_min3_i32 v160, v140, v141, v160
	v_min3_i32 v160, v142, v143, v160
	v_min3_i32 v160, v144, v145, v160
	v_min3_i32 v160, v146, v147, v160
	v_min3_i32 v160, v148, v149, v160
	v_min3_i32 v156, v150, v151, v160
	v_cmp_ge_i32_e32 vcc, v156, v157
	v_mfma_f32_16x16x32_f16 v[136:139], v[64:67], v[112:115], 0
	v_mfma_f32_16x16x32_f16 v[140:143], v[68:71], v[112:115], 0
	v_cndmask_b32_e32 v158, 1, v158, vcc
	v_mfma_f32_16x16x32_f16 v[144:147], v[72:75], v[112:115], 0
	v_mfma_f32_16x16x32_f16 v[148:151], v[76:79], v[112:115], 0
	v_min3_i32 v160, v120, v121, v156
	v_min3_i32 v160, v122, v123, v160
	v_min3_i32 v160, v124, v125, v160
	v_min3_i32 v160, v126, v127, v160
	v_min3_i32 v160, v128, v129, v160
	v_min3_i32 v160, v130, v131, v160
	v_min3_i32 v160, v132, v133, v160
	v_min3_i32 v157, v134, v135, v160
	v_cmp_ge_i32_e32 vcc, v157, v156
	v_mfma_f32_16x16x32_f16 v[120:123], v[80:83], v[112:115], 0
	v_mfma_f32_16x16x32_f16 v[124:127], v[84:87], v[112:115], 0
	v_cndmask_b32_e32 v158, 2, v158, vcc
	v_mfma_f32_16x16x32_f16 v[128:131], v[88:91], v[112:115], 0
	v_mfma_f32_16x16x32_f16 v[132:135], v[92:95], v[112:115], 0
	v_min3_i32 v160, v136, v137, v157
	v_min3_i32 v160, v138, v139, v160
	v_min3_i32 v160, v140, v141, v160
	v_min3_i32 v160, v142, v143, v160
	v_min3_i32 v160, v144, v145, v160
	v_min3_i32 v160, v146, v147, v160
	v_min3_i32 v160, v148, v149, v160
	v_min3_i32 v156, v150, v151, v160
	v_cmp_ge_i32_e32 vcc, v156, v157
	v_mfma_f32_16x16x32_f16 v[136:139], v[96:99], v[112:115], 0
	v_mfma_f32_16x16x32_f16 v[140:143], v[100:103], v[112:115], 0
	v_cndmask_b32_e32 v158, 3, v158, vcc
	v_mfma_f32_16x16x32_f16 v[144:147], v[104:107], v[112:115], 0
	v_mfma_f32_16x16x32_f16 v[148:151], v[108:111], v[112:115], 0
	v_min3_i32 v160, v120, v121, v156
	v_min3_i32 v160, v122, v123, v160
	v_min3_i32 v160, v124, v125, v160
	v_min3_i32 v160, v126, v127, v160
	v_min3_i32 v160, v128, v129, v160
	v_min3_i32 v160, v130, v131, v160
	v_min3_i32 v160, v132, v133, v160
	v_min3_i32 v157, v134, v135, v160
	v_cmp_ge_i32_e32 vcc, v157, v156
	s_nop 1
	v_cndmask_b32_e32 v158, 4, v158, vcc
	s_nop 7
	v_min3_i32 v160, v136, v137, v157
	v_min3_i32 v160, v138, v139, v160
	v_min3_i32 v160, v140, v141, v160
	v_min3_i32 v160, v142, v143, v160
	v_min3_i32 v160, v144, v145, v160
	v_min3_i32 v160, v146, v147, v160
	v_min3_i32 v160, v148, v149, v160
	v_min3_i32 v156, v150, v151, v160
	v_cmp_ge_i32_e32 vcc, v156, v157
	s_nop 1
	v_cndmask_b32_e32 v158, 5, v158, vcc
	v_add_u32_e32 v162, s40, v158
	v_lshl_or_b32 v162, v162, 2, v166
	v_mov_b32_e32 v163, v156
	ds_min_u64 v167, v[162:163] offset:17408
	s_waitcnt lgkmcnt(0)
	s_barrier
	s_add_i32 s65, s50, 4
	s_mov_b32 s66, 8
	s_cmp_ge_u32 s50, 2
	s_cbranch_scc0 .Lq1
	s_lshl_b32 s60, s65, 7
	v_add_u32_e32 v2, s60, v169
	ds_read_b32 v216, v2 offset:16384
	s_lshl_b32 s60, s65, 10
	v_add_u32_e32 v248, s60, v170
.Lq1:
	s_cmp_eq_u32 s50, 0
	s_cbranch_scc0 .Lq2
	s_lshl_b32 s60, s66, 7
	v_add_u32_e32 v2, s60, v169
	ds_read_b32 v16, v2 offset:16384
	s_lshl_b32 s60, s66, 10
	v_add_u32_e32 v48, s60, v170

.Lq4:
	s_lshl_b32 s60, s50, 4
	v_add_u32_e32 v2, s60, v177
	v_mul_u32_u24_e32 v3, 0x556, v2
	v_lshrrev_b32_e32 v3, 16, v3
	v_mul_u32_u24_e32 v4, 48, v3
	v_sub_u32_e32 v4, v2, v4
	v_mul_u32_u24_e32 v3, 0x6c0, v3
	v_mad_u32_u24 v215, v4, 12, v3
	v_add_u32_e32 v215, v215, v175
	s_lshl_b32 s60, s65, 4
	v_add_u32_e32 v2, s60, v177
	v_mul_u32_u24_e32 v3, 0x556, v2
	v_lshrrev_b32_e32 v3, 16, v3
	v_mul_u32_u24_e32 v4, 48, v3
	v_sub_u32_e32 v4, v2, v4
	v_mul_u32_u24_e32 v3, 0x6c0, v3
	v_mad_u32_u24 v253, v4, 12, v3
	v_add_u32_e32 v253, v253, v175
	s_waitcnt vmcnt(9)
	v_mov_b32_e32 v56, 0
	v_mov_b32_e32 v57, 0
	v_dot2c_f32_f16_dpp v56, v210, v178 quad_perm:[0,0,0,0] row_mask:0xf bank_mask:0xf
	v_dot2c_f32_f16_dpp v57, v210, v194 quad_perm:[0,0,0,0] row_mask:0xf bank_mask:0xf
	v_dot2c_f32_f16_dpp v56, v211, v179 quad_perm:[0,0,0,0] row_mask:0xf bank_mask:0xf
	v_dot2c_f32_f16_dpp v57, v211, v195 quad_perm:[0,0,0,0] row_mask:0xf bank_mask:0xf
	v_dot2c_f32_f16_dpp v56, v212, v180 quad_perm:[0,0,0,0] row_mask:0xf bank_mask:0xf
	v_dot2c_f32_f16_dpp v57, v212, v196 quad_perm:[0,0,0,0] row_mask:0xf bank_mask:0xf
	v_dot2c_f32_f16_dpp v56, v213, v181 quad_perm:[0,0,0,0] row_mask:0xf bank_mask:0xf
	v_dot2c_f32_f16_dpp v57, v213, v197 quad_perm:[0,0,0,0] row_mask:0xf bank_mask:0xf
	v_dot2c_f32_f16_dpp v56, v210, v182 quad_perm:[1,1,1,1] row_mask:0xf bank_mask:0xf
	v_dot2c_f32_f16_dpp v57, v210, v198 quad_perm:[1,1,1,1] row_mask:0xf bank_mask:0xf
	v_dot2c_f32_f16_dpp v56, v211, v183 quad_perm:[1,1,1,1] row_mask:0xf bank_mask:0xf
	v_dot2c_f32_f16_dpp v57, v211, v199 quad_perm:[1,1,1,1] row_mask:0xf bank_mask:0xf
	v_dot2c_f32_f16_dpp v56, v212, v184 quad_perm:[1,1,1,1] row_mask:0xf bank_mask:0xf
	v_dot2c_f32_f16_dpp v57, v212, v200 quad_perm:[1,1,1,1] row_mask:0xf bank_mask:0xf
	v_dot2c_f32_f16_dpp v56, v213, v185 quad_perm:[1,1,1,1] row_mask:0xf bank_mask:0xf
	v_dot2c_f32_f16_dpp v57, v213, v201 quad_perm:[1,1,1,1] row_mask:0xf bank_mask:0xf
	v_dot2c_f32_f16_dpp v56, v210, v186 quad_perm:[2,2,2,2] row_mask:0xf bank_mask:0xf
	v_dot2c_f32_f16_dpp v57, v210, v202 quad_perm:[2,2,2,2] row_mask:0xf bank_mask:0xf
	v_dot2c_f32_f16_dpp v56, v211, v187 quad_perm:[2,2,2,2] row_mask:0xf bank_mask:0xf
	v_dot2c_f32_f16_dpp v57, v211, v203 quad_perm:[2,2,2,2] row_mask:0xf bank_mask:0xf
	v_dot2c_f32_f16_dpp v56, v212, v188 quad_perm:[2,2,2,2] row_mask:0xf bank_mask:0xf
	v_dot2c_f32_f16_dpp v57, v212, v204 quad_perm:[2,2,2,2] row_mask:0xf bank_mask:0xf
	v_dot2c_f32_f16_dpp v56, v213, v189 quad_perm:[2,2,2,2] row_mask:0xf bank_mask:0xf
	v_dot2c_f32_f16_dpp v57, v213, v205 quad_perm:[2,2,2,2] row_mask:0xf bank_mask:0xf
	v_dot2c_f32_f16_dpp v56, v210, v190 quad_perm:[3,3,3,3] row_mask:0xf bank_mask:0xf
	v_dot2c_f32_f16_dpp v57, v210, v206 quad_perm:[3,3,3,3] row_mask:0xf bank_mask:0xf
	v_dot2c_f32_f16_dpp v56, v211, v191 quad_perm:[3,3,3,3] row_mask:0xf bank_mask:0xf
	v_dot2c_f32_f16_dpp v57, v211, v207 quad_perm:[3,3,3,3] row_mask:0xf bank_mask:0xf
	v_dot2c_f32_f16_dpp v56, v212, v192 quad_perm:[3,3,3,3] row_mask:0xf bank_mask:0xf
	v_dot2c_f32_f16_dpp v57, v212, v208 quad_perm:[3,3,3,3] row_mask:0xf bank_mask:0xf
	v_dot2c_f32_f16_dpp v56, v213, v193 quad_perm:[3,3,3,3] row_mask:0xf bank_mask:0xf
	v_dot2c_f32_f16_dpp v57, v213, v209 quad_perm:[3,3,3,3] row_mask:0xf bank_mask:0xf
	s_nop 2
	v_and_or_b32 v2, v56, -16, v168
	v_and_or_b32 v3, v57, -16, v176
	v_min_i32_e32 v58, v2, v3
	s_nop 1
	v_min_i32_dpp v58, v58, v58 quad_perm:[1,0,3,2] row_mask:0xf bank_mask:0xf bound_ctrl:1
	s_nop 1
	v_min_i32_dpp v58, v58, v58 quad_perm:[2,3,0,1] row_mask:0xf bank_mask:0xf bound_ctrl:1
	s_nop 1
	v_min_i32_dpp v58, v58, v58 row_half_mirror row_mask:0xf bank_mask:0xf bound_ctrl:1
	v_and_b32_e32 v2, 12, v58
	v_lshlrev_b32_e32 v2, 2, v2
	v_and_b32_e32 v3, 3, v58
	v_sub_u32_e32 v4, v214, v171
	v_add3_u32 v59, v4, v2, v3
	v_cmp_le_u32_e64 s[54:55], s58, v59
	v_cmp_le_u32_e64 s[56:57], s59, v59
	s_nop 1
	v_cndmask_b32_e64 v2, 0, v7, s[54:55]
	v_cndmask_b32_e64 v3, 0, v8, s[56:57]
	v_sub_u32_e32 v4, v59, v2
	v_sub_u32_e32 v4, v4, v3
	v_cndmask_b32_e64 v2, 0, 1, s[54:55]
	v_cndmask_b32_e64 v3, 0, 1, s[56:57]
	v_add_u32_e32 v5, v2, v3
	v_lshlrev_b32_e32 v2, v5, v4
	v_mul_u32_u24_e32 v2, 0xaab, v2
	v_lshrrev_b32_e32 v2, 17, v2
	v_mul_u32_u24_e32 v3, 0x60, v2
	v_lshrrev_b32_e32 v3, v5, v3
	v_add_u32_e32 v3, v4, v3
	v_mul_u32_u24_e32 v3, 12, v3
	v_cndmask_b32_e64 v2, v172, v173, s[54:55]
	v_cndmask_b32_e64 v2, v2, v174, s[56:57]
	v_add_u32_e32 v3, v3, v2
	v_cndmask_b32_e64 v2, v152, v154, s[54:55]
	v_cndmask_b32_e64 v2, v2, v159, s[56:57]
	v_cndmask_b32_e64 v4, v153, v155, s[54:55]
	v_cndmask_b32_e64 v4, v4, v161, s[56:57]
	v_add_co_u32_e64 v60, s[60:61], v2, v3
	s_nop 1
	v_addc_co_u32_e64 v61, s[60:61], 0, v4, s[60:61]
	v_sub_u32_e32 v2, 2, v5
	v_lshlrev_b32_e64 v2, v2, 36
	v_add_u32_e32 v4, 1, v2
	v_mul_u32_u24_e32 v2, v2, v4
	v_lshlrev_b32_e32 v2, 3, v2
	v_add_co_u32_e64 v62, s[60:61], v60, v2
	s_nop 1
	v_addc_co_u32_e64 v63, s[60:61], 0, v61, s[60:61]
	global_load_dwordx3 v[64:66], v[60:61], off
	ds_read_b32 v72, v215
	ds_read_b32 v73, v215 offset:4
	ds_read_b32 v74, v215 offset:8
	s_mov_b64 s[52:53], exec
	s_and_b64 exec, exec, s[48:49]
	global_load_dwordx3 v[68:70], v[62:63], off
	ds_read_b32 v76, v215 offset:11520
	ds_read_b32 v77, v215 offset:11524
	ds_read_b32 v78, v215 offset:11528
	s_mov_b64 exec, s[52:53]
	s_waitcnt vmcnt(2)
	v_mov_b32_e32 v84, 0
	v_mov_b32_e32 v85, 0
	v_dot2c_f32_f16_dpp v84, v248, v216 quad_perm:[0,0,0,0] row_mask:0xf bank_mask:0xf
	v_dot2c_f32_f16_dpp v85, v248, v232 quad_perm:[0,0,0,0] row_mask:0xf bank_mask:0xf
	v_dot2c_f32_f16_dpp v84, v249, v217 quad_perm:[0,0,0,0] row_mask:0xf bank_mask:0xf
	v_dot2c_f32_f16_dpp v85, v249, v233 quad_perm:[0,0,0,0] row_mask:0xf bank_mask:0xf
	v_dot2c_f32_f16_dpp v84, v250, v218 quad_perm:[0,0,0,0] row_mask:0xf bank_mask:0xf
	v_dot2c_f32_f16_dpp v85, v250, v234 quad_perm:[0,0,0,0] row_mask:0xf bank_mask:0xf
	v_dot2c_f32_f16_dpp v84, v251, v219 quad_perm:[0,0,0,0] row_mask:0xf bank_mask:0xf
	v_dot2c_f32_f16_dpp v85, v251, v235 quad_perm:[0,0,0,0] row_mask:0xf bank_mask:0xf
	v_dot2c_f32_f16_dpp v84, v248, v220 quad_perm:[1,1,1,1] row_mask:0xf bank_mask:0xf
	v_dot2c_f32_f16_dpp v85, v248, v236 quad_perm:[1,1,1,1] row_mask:0xf bank_mask:0xf
	v_dot2c_f32_f16_dpp v84, v249, v221 quad_perm:[1,1,1,1] row_mask:0xf bank_mask:0xf
	v_dot2c_f32_f16_dpp v85, v249, v237 quad_perm:[1,1,1,1] row_mask:0xf bank_mask:0xf
	v_dot2c_f32_f16_dpp v84, v250, v222 quad_perm:[1,1,1,1] row_mask:0xf bank_mask:0xf
	v_dot2c_f32_f16_dpp v85, v250, v238 quad_perm:[1,1,1,1] row_mask:0xf bank_mask:0xf
	v_dot2c_f32_f16_dpp v84, v251, v223 quad_perm:[1,1,1,1] row_mask:0xf bank_mask:0xf
	v_dot2c_f32_f16_dpp v85, v251, v239 quad_perm:[1,1,1,1] row_mask:0xf bank_mask:0xf
	v_dot2c_f32_f16_dpp v84, v248, v224 quad_perm:[2,2,2,2] row_mask:0xf bank_mask:0xf
	v_dot2c_f32_f16_dpp v85, v248, v240 quad_perm:[2,2,2,2] row_mask:0xf bank_mask:0xf
	v_dot2c_f32_f16_dpp v84, v249, v225 quad_perm:[2,2,2,2] row_mask:0xf bank_mask:0xf
	v_dot2c_f32_f16_dpp v85, v249, v241 quad_perm:[2,2,2,2] row_mask:0xf bank_mask:0xf
	v_dot2c_f32_f16_dpp v84, v250, v226 quad_perm:[2,2,2,2] row_mask:0xf bank_mask:0xf
	v_dot2c_f32_f16_dpp v85, v250, v242 quad_perm:[2,2,2,2] row_mask:0xf bank_mask:0xf
	v_dot2c_f32_f16_dpp v84, v251, v227 quad_perm:[2,2,2,2] row_mask:0xf bank_mask:0xf
	v_dot2c_f32_f16_dpp v85, v251, v243 quad_perm:[2,2,2,2] row_mask:0xf bank_mask:0xf
	v_dot2c_f32_f16_dpp v84, v248, v228 quad_perm:[3,3,3,3] row_mask:0xf bank_mask:0xf
	v_dot2c_f32_f16_dpp v85, v248, v244 quad_perm:[3,3,3,3] row_mask:0xf bank_mask:0xf
	v_dot2c_f32_f16_dpp v84, v249, v229 quad_perm:[3,3,3,3] row_mask:0xf bank_mask:0xf
	v_dot2c_f32_f16_dpp v85, v249, v245 quad_perm:[3,3,3,3] row_mask:0xf bank_mask:0xf
	v_dot2c_f32_f16_dpp v84, v250, v230 quad_perm:[3,3,3,3] row_mask:0xf bank_mask:0xf
	v_dot2c_f32_f16_dpp v85, v250, v246 quad_perm:[3,3,3,3] row_mask:0xf bank_mask:0xf
	v_dot2c_f32_f16_dpp v84, v251, v231 quad_perm:[3,3,3,3] row_mask:0xf bank_mask:0xf
	v_dot2c_f32_f16_dpp v85, v251, v247 quad_perm:[3,3,3,3] row_mask:0xf bank_mask:0xf
	s_nop 2
	v_and_or_b32 v2, v84, -16, v168
	v_and_or_b32 v3, v85, -16, v176
	v_min_i32_e32 v86, v2, v3
	s_nop 1
	v_min_i32_dpp v86, v86, v86 quad_perm:[1,0,3,2] row_mask:0xf bank_mask:0xf bound_ctrl:1
	s_nop 1
	v_min_i32_dpp v86, v86, v86 quad_perm:[2,3,0,1] row_mask:0xf bank_mask:0xf bound_ctrl:1
	s_nop 1
	v_min_i32_dpp v86, v86, v86 row_half_mirror row_mask:0xf bank_mask:0xf bound_ctrl:1
	v_and_b32_e32 v2, 12, v86
	v_lshlrev_b32_e32 v2, 2, v2
	v_and_b32_e32 v3, 3, v86
	v_sub_u32_e32 v4, v252, v171
	v_add3_u32 v87, v4, v2, v3
	v_cmp_le_u32_e64 s[54:55], s58, v87
	v_cmp_le_u32_e64 s[56:57], s59, v87
	s_nop 1
	v_cndmask_b32_e64 v2, 0, v7, s[54:55]
	v_cndmask_b32_e64 v3, 0, v8, s[56:57]
	v_sub_u32_e32 v4, v87, v2
	v_sub_u32_e32 v4, v4, v3
	v_cndmask_b32_e64 v2, 0, 1, s[54:55]
	v_cndmask_b32_e64 v3, 0, 1, s[56:57]
	v_add_u32_e32 v5, v2, v3
	v_lshlrev_b32_e32 v2, v5, v4
	v_mul_u32_u24_e32 v2, 0xaab, v2
	v_lshrrev_b32_e32 v2, 17, v2
	v_mul_u32_u24_e32 v3, 0x60, v2
	v_lshrrev_b32_e32 v3, v5, v3
	v_add_u32_e32 v3, v4, v3
	v_mul_u32_u24_e32 v3, 12, v3
	v_cndmask_b32_e64 v2, v172, v173, s[54:55]
	v_cndmask_b32_e64 v2, v2, v174, s[56:57]
	v_add_u32_e32 v3, v3, v2
	v_cndmask_b32_e64 v2, v152, v154, s[54:55]
	v_cndmask_b32_e64 v2, v2, v159, s[56:57]
	v_cndmask_b32_e64 v4, v153, v155, s[54:55]
	v_cndmask_b32_e64 v4, v4, v161, s[56:57]
	v_add_co_u32_e64 v88, s[60:61], v2, v3
	s_nop 1
	v_addc_co_u32_e64 v89, s[60:61], 0, v4, s[60:61]
	v_sub_u32_e32 v2, 2, v5
	v_lshlrev_b32_e64 v2, v2, 36
	v_add_u32_e32 v4, 1, v2
	v_mul_u32_u24_e32 v2, v2, v4
	v_lshlrev_b32_e32 v2, 3, v2
	v_add_co_u32_e64 v90, s[60:61], v88, v2
	s_nop 1
	v_addc_co_u32_e64 v91, s[60:61], 0, v89, s[60:61]
	global_load_dwordx3 v[92:94], v[88:89], off
	ds_read_b32 v100, v253
	ds_read_b32 v101, v253 offset:4
	ds_read_b32 v102, v253 offset:8
	s_mov_b64 s[52:53], exec
	s_and_b64 exec, exec, s[48:49]
	global_load_dwordx3 v[96:98], v[90:91], off
	ds_read_b32 v104, v253 offset:11520
	ds_read_b32 v105, v253 offset:11524
	ds_read_b32 v106, v253 offset:11528
	s_mov_b64 exec, s[52:53]
	s_cmp_eq_u32 s50, 0
	s_cbranch_scc0 .Lq5
	s_lshl_b32 s60, s66, 4
	v_add_u32_e32 v2, s60, v177
	v_mul_u32_u24_e32 v3, 0x556, v2
	v_lshrrev_b32_e32 v3, 16, v3
	v_mul_u32_u24_e32 v4, 48, v3
	v_sub_u32_e32 v4, v2, v4
	v_mul_u32_u24_e32 v3, 0x6c0, v3
	v_mad_u32_u24 v53, v4, 12, v3
	v_add_u32_e32 v53, v53, v175
	s_waitcnt vmcnt(4)
	v_mov_b32_e32 v112, 0
	v_mov_b32_e32 v113, 0
	v_dot2c_f32_f16_dpp v112, v48, v16 quad_perm:[0,0,0,0] row_mask:0xf bank_mask:0xf
	v_dot2c_f32_f16_dpp v113, v48, v32 quad_perm:[0,0,0,0] row_mask:0xf bank_mask:0xf
	v_dot2c_f32_f16_dpp v112, v49, v17 quad_perm:[0,0,0,0] row_mask:0xf bank_mask:0xf
	v_dot2c_f32_f16_dpp v113, v49, v33 quad_perm:[0,0,0,0] row_mask:0xf bank_mask:0xf
	v_dot2c_f32_f16_dpp v112, v50, v18 quad_perm:[0,0,0,0] row_mask:0xf bank_mask:0xf
	v_dot2c_f32_f16_dpp v113, v50, v34 quad_perm:[0,0,0,0] row_mask:0xf bank_mask:0xf
	v_dot2c_f32_f16_dpp v112, v51, v19 quad_perm:[0,0,0,0] row_mask:0xf bank_mask:0xf
	v_dot2c_f32_f16_dpp v113, v51, v35 quad_perm:[0,0,0,0] row_mask:0xf bank_mask:0xf
	v_dot2c_f32_f16_dpp v112, v48, v20 quad_perm:[1,1,1,1] row_mask:0xf bank_mask:0xf
	v_dot2c_f32_f16_dpp v113, v48, v36 quad_perm:[1,1,1,1] row_mask:0xf bank_mask:0xf
	v_dot2c_f32_f16_dpp v112, v49, v21 quad_perm:[1,1,1,1] row_mask:0xf bank_mask:0xf
	v_dot2c_f32_f16_dpp v113, v49, v37 quad_perm:[1,1,1,1] row_mask:0xf bank_mask:0xf
	v_dot2c_f32_f16_dpp v112, v50, v22 quad_perm:[1,1,1,1] row_mask:0xf bank_mask:0xf
	v_dot2c_f32_f16_dpp v113, v50, v38 quad_perm:[1,1,1,1] row_mask:0xf bank_mask:0xf
	v_dot2c_f32_f16_dpp v112, v51, v23 quad_perm:[1,1,1,1] row_mask:0xf bank_mask:0xf
	v_dot2c_f32_f16_dpp v113, v51, v39 quad_perm:[1,1,1,1] row_mask:0xf bank_mask:0xf
	v_dot2c_f32_f16_dpp v112, v48, v24 quad_perm:[2,2,2,2] row_mask:0xf bank_mask:0xf
	v_dot2c_f32_f16_dpp v113, v48, v40 quad_perm:[2,2,2,2] row_mask:0xf bank_mask:0xf
	v_dot2c_f32_f16_dpp v112, v49, v25 quad_perm:[2,2,2,2] row_mask:0xf bank_mask:0xf
	v_dot2c_f32_f16_dpp v113, v49, v41 quad_perm:[2,2,2,2] row_mask:0xf bank_mask:0xf
	v_dot2c_f32_f16_dpp v112, v50, v26 quad_perm:[2,2,2,2] row_mask:0xf bank_mask:0xf
	v_dot2c_f32_f16_dpp v113, v50, v42 quad_perm:[2,2,2,2] row_mask:0xf bank_mask:0xf
	v_dot2c_f32_f16_dpp v112, v51, v27 quad_perm:[2,2,2,2] row_mask:0xf bank_mask:0xf
	v_dot2c_f32_f16_dpp v113, v51, v43 quad_perm:[2,2,2,2] row_mask:0xf bank_mask:0xf
	v_dot2c_f32_f16_dpp v112, v48, v28 quad_perm:[3,3,3,3] row_mask:0xf bank_mask:0xf
	v_dot2c_f32_f16_dpp v113, v48, v44 quad_perm:[3,3,3,3] row_mask:0xf bank_mask:0xf
	v_dot2c_f32_f16_dpp v112, v49, v29 quad_perm:[3,3,3,3] row_mask:0xf bank_mask:0xf
	v_dot2c_f32_f16_dpp v113, v49, v45 quad_perm:[3,3,3,3] row_mask:0xf bank_mask:0xf
	v_dot2c_f32_f16_dpp v112, v50, v30 quad_perm:[3,3,3,3] row_mask:0xf bank_mask:0xf
	v_dot2c_f32_f16_dpp v113, v50, v46 quad_perm:[3,3,3,3] row_mask:0xf bank_mask:0xf
	v_dot2c_f32_f16_dpp v112, v51, v31 quad_perm:[3,3,3,3] row_mask:0xf bank_mask:0xf
	v_dot2c_f32_f16_dpp v113, v51, v47 quad_perm:[3,3,3,3] row_mask:0xf bank_mask:0xf
	s_nop 2
	v_and_or_b32 v2, v112, -16, v168
	v_and_or_b32 v3, v113, -16, v176
	v_min_i32_e32 v114, v2, v3
	s_nop 1
	v_min_i32_dpp v114, v114, v114 quad_perm:[1,0,3,2] row_mask:0xf bank_mask:0xf bound_ctrl:1
	s_nop 1
	v_min_i32_dpp v114, v114, v114 quad_perm:[2,3,0,1] row_mask:0xf bank_mask:0xf bound_ctrl:1
	s_nop 1
	v_min_i32_dpp v114, v114, v114 row_half_mirror row_mask:0xf bank_mask:0xf bound_ctrl:1
	v_and_b32_e32 v2, 12, v114
	v_lshlrev_b32_e32 v2, 2, v2
	v_and_b32_e32 v3, 3, v114
	v_sub_u32_e32 v4, v52, v171
	v_add3_u32 v115, v4, v2, v3
	v_cmp_le_u32_e64 s[54:55], s58, v115
	v_cmp_le_u32_e64 s[56:57], s59, v115
	s_nop 1
	v_cndmask_b32_e64 v2, 0, v7, s[54:55]
	v_cndmask_b32_e64 v3, 0, v8, s[56:57]
	v_sub_u32_e32 v4, v115, v2
	v_sub_u32_e32 v4, v4, v3
	v_cndmask_b32_e64 v2, 0, 1, s[54:55]
	v_cndmask_b32_e64 v3, 0, 1, s[56:57]
	v_add_u32_e32 v5, v2, v3
	v_lshlrev_b32_e32 v2, v5, v4
	v_mul_u32_u24_e32 v2, 0xaab, v2
	v_lshrrev_b32_e32 v2, 17, v2
	v_mul_u32_u24_e32 v3, 0x60, v2
	v_lshrrev_b32_e32 v3, v5, v3
	v_add_u32_e32 v3, v4, v3
	v_mul_u32_u24_e32 v3, 12, v3
	v_cndmask_b32_e64 v2, v172, v173, s[54:55]
	v_cndmask_b32_e64 v2, v2, v174, s[56:57]
	v_add_u32_e32 v3, v3, v2
	v_cndmask_b32_e64 v2, v152, v154, s[54:55]
	v_cndmask_b32_e64 v2, v2, v159, s[56:57]
	v_cndmask_b32_e64 v4, v153, v155, s[54:55]
	v_cndmask_b32_e64 v4, v4, v161, s[56:57]
	v_add_co_u32_e64 v116, s[60:61], v2, v3
	s_nop 1
	v_addc_co_u32_e64 v117, s[60:61], 0, v4, s[60:61]
	v_sub_u32_e32 v2, 2, v5
	v_lshlrev_b32_e64 v2, v2, 36
	v_add_u32_e32 v4, 1, v2
	v_mul_u32_u24_e32 v2, v2, v4
	v_lshlrev_b32_e32 v2, 3, v2
	v_add_co_u32_e64 v118, s[60:61], v116, v2
	s_nop 1
	v_addc_co_u32_e64 v119, s[60:61], 0, v117, s[60:61]
	global_load_dwordx3 v[120:122], v[116:117], off
	ds_read_b32 v128, v53
	ds_read_b32 v129, v53 offset:4
	ds_read_b32 v130, v53 offset:8
	s_mov_b64 s[52:53], exec
	s_and_b64 exec, exec, s[48:49]
	global_load_dwordx3 v[124:126], v[118:119], off
	ds_read_b32 v132, v53 offset:11520
	ds_read_b32 v133, v53 offset:11524
	ds_read_b32 v134, v53 offset:11528
	s_mov_b64 exec, s[52:53]
